# baseline (speedup 1.0000x reference)
_Z5k_decPKiPKDF16_S2_PKfS4_S4_Pf:
	s_load_dword s3, s[0:1], 0x44
	s_load_dword s6, s[0:1], 0x38
	s_load_dwordx2 s[4:5], s[0:1], 0x0
	s_load_dwordx8 s[28:35], s[0:1], 0x8
	s_load_dwordx4 s[12:15], s[0:1], 0x28
	v_and_b32_e32 v1, 15, v0
	v_and_b32_e32 v64, 63, v0
	v_lshlrev_b32_e32 v96, 3, v1
	v_lshrrev_b32_e32 v4, 3, v0
	v_and_b32_e32 v4, 4, v4
	v_or_b32_e32 v96, v96, v4
	v_mov_b32_e32 v97, 0
	v_and_b32_e32 v104, 16, v0
	v_lshlrev_b32_e32 v6, 7, v0
	v_lshlrev_b32_e32 v7, 2, v64
	s_movk_i32 s16, 0x6000
	v_and_or_b32 v103, v6, s16, v7
	v_mov_b32_e32 v219, 0
	s_movk_i32 s19, 0x3d08
	s_waitcnt lgkmcnt(0)
	s_and_b32 s3, s3, 0xffff
	s_mul_i32 s2, s2, s3
	v_add_u32_e32 v5, s2, v0
	s_mul_i32 s6, s6, s3
	v_lshrrev_b32_e32 v102, 6, v5
	s_lshr_b32 s18, s6, 6
	v_readfirstlane_b32 s23, v102
	v_lshl_add_u64 v[2:3], s[4:5], 0, v[96:97]
	s_mov_b32 s16, 0xf4240
	v_cmp_gt_u32_e32 vcc, s16, v5
	s_and_saveexec_b64 s[22:23], vcc
	s_cbranch_execz .LBB2_3
	v_mov_b32_e32 v222, v2
	v_mov_b32_e32 v223, v3
	v_min_u32_e32 v218, s19, v102
	v_lshlrev_b32_e32 v218, 9, v218
	v_lshl_add_u64 v[216:217], v[222:223], 0, v[218:219]
	global_load_dword v65, v[216:217], off
	global_load_dword v80, v[216:217], off offset:128
	global_load_dword v81, v[216:217], off offset:256
	global_load_dword v82, v[216:217], off offset:384
	v_add_u32_e32 v220, s18, v102
	v_min_u32_e32 v218, s19, v220
	v_lshlrev_b32_e32 v218, 9, v218
	v_lshl_add_u64 v[216:217], v[222:223], 0, v[218:219]
	global_load_dword v100, v[216:217], off
	global_load_dword v101, v[216:217], off offset:128
	global_load_dword v98, v[216:217], off offset:256
	global_load_dword v99, v[216:217], off offset:384
	s_mov_b32 s8, s28
	s_and_b32 s9, s29, 0xffff
	s_mov_b32 s10, 0x30d400
	s_mov_b32 s11, 0x20000
	s_mov_b64 s[36:37], 0x1000
	v_and_b32_e32 v96, 48, v64
	v_lshlrev_b32_e32 v221, 6, v1
	v_lshlrev_b32_e32 v211, 2, v1
	v_mov_b32_e32 v214, v221
	v_mov_b32_e32 v215, 0
	v_lshl_add_u64 v[216:217], s[30:31], 0, v[96:97]
	v_lshl_add_u64 v[48:49], v[216:217], 0, v[214:215]
	v_lshl_add_u64 v[66:67], v[48:49], 0, s[36:37]
	v_lshl_or_b32 v221, v102, 6, v64
	v_lshrrev_b32_e32 v213, 4, v64
	v_cmp_gt_u32_e32 vcc, 16, v64
	global_load_dwordx4 v[68:71], v96, s[34:35]
	global_load_dwordx4 v[0:3], v96, s[32:33]
	global_load_dwordx4 v[72:75], v96, s[34:35] offset:64
	global_load_dwordx4 v[4:7], v96, s[32:33] offset:64
	global_load_dwordx4 v[76:79], v96, s[34:35] offset:128
	global_load_dwordx4 v[8:11], v96, s[32:33] offset:128
	global_load_dwordx4 v[106:109], v96, s[34:35] offset:192
	global_load_dwordx4 v[12:15], v96, s[32:33] offset:192
	global_load_dwordx4 v[110:113], v96, s[34:35] offset:256
	global_load_dwordx4 v[16:19], v96, s[32:33] offset:256
	global_load_dwordx4 v[114:117], v96, s[34:35] offset:320
	global_load_dwordx4 v[20:23], v96, s[32:33] offset:320
	global_load_dwordx4 v[118:121], v96, s[34:35] offset:384
	global_load_dwordx4 v[24:27], v96, s[32:33] offset:384
	global_load_dwordx4 v[122:125], v96, s[34:35] offset:448
	global_load_dwordx4 v[28:31], v96, s[32:33] offset:448
	global_load_dwordx4 v[32:35], v[48:49], off
	global_load_dwordx4 v[36:39], v[48:49], off offset:1024
	global_load_dwordx4 v[40:43], v[48:49], off offset:2048
	global_load_dwordx4 v[44:47], v[48:49], off offset:3072
	s_nop 0
	global_load_dwordx4 v[48:51], v[66:67], off
	global_load_dwordx4 v[52:55], v[66:67], off offset:1024
	global_load_dwordx4 v[56:59], v[66:67], off offset:2048
	global_load_dwordx4 v[60:63], v[66:67], off offset:3072
	global_load_dword v148, v211, s[34:35]
	global_load_dword v156, v211, s[32:33]
	global_load_dword v149, v211, s[34:35] offset:64
	global_load_dword v157, v211, s[32:33] offset:64
	global_load_dword v150, v211, s[34:35] offset:128
	global_load_dword v158, v211, s[32:33] offset:128
	global_load_dword v151, v211, s[34:35] offset:192
	global_load_dword v159, v211, s[32:33] offset:192
	global_load_dword v152, v211, s[34:35] offset:256
	global_load_dword v160, v211, s[32:33] offset:256
	global_load_dword v153, v211, s[34:35] offset:320
	global_load_dword v161, v211, s[32:33] offset:320
	global_load_dword v154, v211, s[34:35] offset:384
	global_load_dword v162, v211, s[32:33] offset:384
	global_load_dword v155, v211, s[34:35] offset:448
	global_load_dword v163, v211, s[32:33] offset:448
	s_load_dword s12, s[12:13], 0x0
	s_waitcnt vmcnt(44)
	v_lshl_or_b32 v216, v65, 5, v104
	v_lshl_or_b32 v217, v80, 5, v104
	v_lshl_or_b32 v218, v81, 5, v104
	v_lshl_or_b32 v212, v82, 5, v104
	buffer_load_dwordx4 v[92:95], v216, s[8:11], 0 offen
	buffer_load_dwordx4 v[88:91], v217, s[8:11], 0 offen
	buffer_load_dwordx4 v[84:87], v218, s[8:11], 0 offen
	buffer_load_dwordx4 v[80:83], v212, s[8:11], 0 offen
	s_lshl_b32 s21, s18, 6
	s_mov_b32 s20, 2
	s_mov_b64 s[16:17], 0
	v_cmp_eq_u32_e64 s[0:1], 1, v213
	v_cmp_eq_u32_e64 s[2:3], 2, v213
	v_cmp_eq_u32_e64 s[4:5], 3, v213
	v_mov_b32_e32 v96, v221
	v_mov_b32_e32 v97, 0
	s_waitcnt vmcnt(4)
	v_cvt_pk_f16_f32 v67, v74, v75
	v_cvt_pk_f16_f32 v66, v72, v73
	v_cvt_pk_f16_f32 v65, v70, v71
	v_cvt_pk_f16_f32 v64, v68, v69
	v_cvt_pk_f16_f32 v71, v108, v109
	v_cvt_pk_f16_f32 v70, v106, v107
	v_cvt_pk_f16_f32 v69, v78, v79
	v_cvt_pk_f16_f32 v68, v76, v77
	v_cvt_pk_f16_f32 v75, v116, v117
	v_cvt_pk_f16_f32 v74, v114, v115
	v_cvt_pk_f16_f32 v73, v112, v113
	v_cvt_pk_f16_f32 v72, v110, v111
	v_cvt_pk_f16_f32 v79, v124, v125
	v_cvt_pk_f16_f32 v78, v122, v123
	v_cvt_pk_f16_f32 v77, v120, v121
	v_cvt_pk_f16_f32 v76, v118, v119
	v_mov_b32_e32 v167, 0x38003800
	v_pk_mul_f16 v64, v64, v167
	v_pk_mul_f16 v65, v65, v167
	v_pk_mul_f16 v66, v66, v167
	v_pk_mul_f16 v67, v67, v167
	v_pk_mul_f16 v68, v68, v167
	v_pk_mul_f16 v69, v69, v167
	v_pk_mul_f16 v70, v70, v167
	v_pk_mul_f16 v71, v71, v167
	v_pk_mul_f16 v72, v72, v167
	v_pk_mul_f16 v73, v73, v167
	v_pk_mul_f16 v74, v74, v167
	v_pk_mul_f16 v75, v75, v167
	v_pk_mul_f16 v76, v76, v167
	v_pk_mul_f16 v77, v77, v167
	v_pk_mul_f16 v78, v78, v167
	v_pk_mul_f16 v79, v79, v167
	v_cvt_f16_f32_e32 v148, v148
	v_cvt_f16_f32_e32 v149, v149
	v_cvt_f16_f32_e32 v150, v150
	v_cvt_f16_f32_e32 v151, v151
	v_cvt_f16_f32_e32 v152, v152
	v_cvt_f16_f32_e32 v153, v153
	v_cvt_f16_f32_e32 v154, v154
	v_cvt_f16_f32_e32 v155, v155
	v_cvt_f32_f16_e32 v148, v148
	v_cvt_f32_f16_e32 v149, v149
	v_cvt_f32_f16_e32 v150, v150
	v_cvt_f32_f16_e32 v151, v151
	v_cvt_f32_f16_e32 v152, v152
	v_cvt_f32_f16_e32 v153, v153
	v_cvt_f32_f16_e32 v154, v154
	v_cvt_f32_f16_e32 v155, v155
	v_mul_f32_e32 v148, 0.5, v148
	v_mul_f32_e32 v149, 0.5, v149
	v_mul_f32_e32 v150, 0.5, v150
	v_mul_f32_e32 v151, 0.5, v151
	v_mul_f32_e32 v152, 0.5, v152
	v_mul_f32_e32 v153, 0.5, v153
	v_mul_f32_e32 v154, 0.5, v154
	v_mul_f32_e32 v155, 0.5, v155
	v_mov_b32_e32 v140, 0
	v_mov_b32_e32 v141, 0
	v_mov_b32_e32 v142, 0
	v_mov_b32_e32 v143, 0
	v_mov_b32_e32 v144, 0
	v_mov_b32_e32 v145, 0
	v_mov_b32_e32 v146, 0
	v_mov_b32_e32 v147, 0
	v_mov_b32_e32 v166, 0
	v_cvt_f32_f16_e32 v164, v32
	v_cvt_f32_f16_sdwa v165, v32 dst_sel:DWORD dst_unused:UNUSED_PAD src0_sel:WORD_1
	v_fmac_f32_e32 v140, v148, v164
	v_fmac_f32_e32 v141, v148, v165
	v_cvt_f32_f16_e32 v164, v33
	v_cvt_f32_f16_sdwa v165, v33 dst_sel:DWORD dst_unused:UNUSED_PAD src0_sel:WORD_1
	v_fmac_f32_e32 v142, v148, v164
	v_fmac_f32_e32 v143, v148, v165
	v_cvt_f32_f16_e32 v164, v34
	v_cvt_f32_f16_sdwa v165, v34 dst_sel:DWORD dst_unused:UNUSED_PAD src0_sel:WORD_1
	v_fmac_f32_e32 v144, v148, v164
	v_fmac_f32_e32 v145, v148, v165
	v_cvt_f32_f16_e32 v164, v35
	v_cvt_f32_f16_sdwa v165, v35 dst_sel:DWORD dst_unused:UNUSED_PAD src0_sel:WORD_1
	v_fmac_f32_e32 v146, v148, v164
	v_fmac_f32_e32 v147, v148, v165
	v_fmac_f32_e32 v166, v148, v156
	v_cvt_f32_f16_e32 v164, v36
	v_cvt_f32_f16_sdwa v165, v36 dst_sel:DWORD dst_unused:UNUSED_PAD src0_sel:WORD_1
	v_fmac_f32_e32 v140, v149, v164
	v_fmac_f32_e32 v141, v149, v165
	v_cvt_f32_f16_e32 v164, v37
	v_cvt_f32_f16_sdwa v165, v37 dst_sel:DWORD dst_unused:UNUSED_PAD src0_sel:WORD_1
	v_fmac_f32_e32 v142, v149, v164
	v_fmac_f32_e32 v143, v149, v165
	v_cvt_f32_f16_e32 v164, v38
	v_cvt_f32_f16_sdwa v165, v38 dst_sel:DWORD dst_unused:UNUSED_PAD src0_sel:WORD_1
	v_fmac_f32_e32 v144, v149, v164
	v_fmac_f32_e32 v145, v149, v165
	v_cvt_f32_f16_e32 v164, v39
	v_cvt_f32_f16_sdwa v165, v39 dst_sel:DWORD dst_unused:UNUSED_PAD src0_sel:WORD_1
	v_fmac_f32_e32 v146, v149, v164
	v_fmac_f32_e32 v147, v149, v165
	v_fmac_f32_e32 v166, v149, v157
	v_cvt_f32_f16_e32 v164, v40
	v_cvt_f32_f16_sdwa v165, v40 dst_sel:DWORD dst_unused:UNUSED_PAD src0_sel:WORD_1
	v_fmac_f32_e32 v140, v150, v164
	v_fmac_f32_e32 v141, v150, v165
	v_cvt_f32_f16_e32 v164, v41
	v_cvt_f32_f16_sdwa v165, v41 dst_sel:DWORD dst_unused:UNUSED_PAD src0_sel:WORD_1
	v_fmac_f32_e32 v142, v150, v164
	v_fmac_f32_e32 v143, v150, v165
	v_cvt_f32_f16_e32 v164, v42
	v_cvt_f32_f16_sdwa v165, v42 dst_sel:DWORD dst_unused:UNUSED_PAD src0_sel:WORD_1
	v_fmac_f32_e32 v144, v150, v164
	v_fmac_f32_e32 v145, v150, v165
	v_cvt_f32_f16_e32 v164, v43
	v_cvt_f32_f16_sdwa v165, v43 dst_sel:DWORD dst_unused:UNUSED_PAD src0_sel:WORD_1
	v_fmac_f32_e32 v146, v150, v164
	v_fmac_f32_e32 v147, v150, v165
	v_fmac_f32_e32 v166, v150, v158
	v_cvt_f32_f16_e32 v164, v44
	v_cvt_f32_f16_sdwa v165, v44 dst_sel:DWORD dst_unused:UNUSED_PAD src0_sel:WORD_1
	v_fmac_f32_e32 v140, v151, v164
	v_fmac_f32_e32 v141, v151, v165
	v_cvt_f32_f16_e32 v164, v45
	v_cvt_f32_f16_sdwa v165, v45 dst_sel:DWORD dst_unused:UNUSED_PAD src0_sel:WORD_1
	v_fmac_f32_e32 v142, v151, v164
	v_fmac_f32_e32 v143, v151, v165
	v_cvt_f32_f16_e32 v164, v46
	v_cvt_f32_f16_sdwa v165, v46 dst_sel:DWORD dst_unused:UNUSED_PAD src0_sel:WORD_1
	v_fmac_f32_e32 v144, v151, v164
	v_fmac_f32_e32 v145, v151, v165
	v_cvt_f32_f16_e32 v164, v47
	v_cvt_f32_f16_sdwa v165, v47 dst_sel:DWORD dst_unused:UNUSED_PAD src0_sel:WORD_1
	v_fmac_f32_e32 v146, v151, v164
	v_fmac_f32_e32 v147, v151, v165
	v_fmac_f32_e32 v166, v151, v159
	v_cvt_f32_f16_e32 v164, v48
	v_cvt_f32_f16_sdwa v165, v48 dst_sel:DWORD dst_unused:UNUSED_PAD src0_sel:WORD_1
	v_fmac_f32_e32 v140, v152, v164
	v_fmac_f32_e32 v141, v152, v165
	v_cvt_f32_f16_e32 v164, v49
	v_cvt_f32_f16_sdwa v165, v49 dst_sel:DWORD dst_unused:UNUSED_PAD src0_sel:WORD_1
	v_fmac_f32_e32 v142, v152, v164
	v_fmac_f32_e32 v143, v152, v165
	v_cvt_f32_f16_e32 v164, v50
	v_cvt_f32_f16_sdwa v165, v50 dst_sel:DWORD dst_unused:UNUSED_PAD src0_sel:WORD_1
	v_fmac_f32_e32 v144, v152, v164
	v_fmac_f32_e32 v145, v152, v165
	v_cvt_f32_f16_e32 v164, v51
	v_cvt_f32_f16_sdwa v165, v51 dst_sel:DWORD dst_unused:UNUSED_PAD src0_sel:WORD_1
	v_fmac_f32_e32 v146, v152, v164
	v_fmac_f32_e32 v147, v152, v165
	v_fmac_f32_e32 v166, v152, v160
	v_cvt_f32_f16_e32 v164, v52
	v_cvt_f32_f16_sdwa v165, v52 dst_sel:DWORD dst_unused:UNUSED_PAD src0_sel:WORD_1
	v_fmac_f32_e32 v140, v153, v164
	v_fmac_f32_e32 v141, v153, v165
	v_cvt_f32_f16_e32 v164, v53
	v_cvt_f32_f16_sdwa v165, v53 dst_sel:DWORD dst_unused:UNUSED_PAD src0_sel:WORD_1
	v_fmac_f32_e32 v142, v153, v164
	v_fmac_f32_e32 v143, v153, v165
	v_cvt_f32_f16_e32 v164, v54
	v_cvt_f32_f16_sdwa v165, v54 dst_sel:DWORD dst_unused:UNUSED_PAD src0_sel:WORD_1
	v_fmac_f32_e32 v144, v153, v164
	v_fmac_f32_e32 v145, v153, v165
	v_cvt_f32_f16_e32 v164, v55
	v_cvt_f32_f16_sdwa v165, v55 dst_sel:DWORD dst_unused:UNUSED_PAD src0_sel:WORD_1
	v_fmac_f32_e32 v146, v153, v164
	v_fmac_f32_e32 v147, v153, v165
	v_fmac_f32_e32 v166, v153, v161
	v_cvt_f32_f16_e32 v164, v56
	v_cvt_f32_f16_sdwa v165, v56 dst_sel:DWORD dst_unused:UNUSED_PAD src0_sel:WORD_1
	v_fmac_f32_e32 v140, v154, v164
	v_fmac_f32_e32 v141, v154, v165
	v_cvt_f32_f16_e32 v164, v57
	v_cvt_f32_f16_sdwa v165, v57 dst_sel:DWORD dst_unused:UNUSED_PAD src0_sel:WORD_1
	v_fmac_f32_e32 v142, v154, v164
	v_fmac_f32_e32 v143, v154, v165
	v_cvt_f32_f16_e32 v164, v58
	v_cvt_f32_f16_sdwa v165, v58 dst_sel:DWORD dst_unused:UNUSED_PAD src0_sel:WORD_1
	v_fmac_f32_e32 v144, v154, v164
	v_fmac_f32_e32 v145, v154, v165
	v_cvt_f32_f16_e32 v164, v59
	v_cvt_f32_f16_sdwa v165, v59 dst_sel:DWORD dst_unused:UNUSED_PAD src0_sel:WORD_1
	v_fmac_f32_e32 v146, v154, v164
	v_fmac_f32_e32 v147, v154, v165
	v_fmac_f32_e32 v166, v154, v162
	v_cvt_f32_f16_e32 v164, v60
	v_cvt_f32_f16_sdwa v165, v60 dst_sel:DWORD dst_unused:UNUSED_PAD src0_sel:WORD_1
	v_fmac_f32_e32 v140, v155, v164
	v_fmac_f32_e32 v141, v155, v165
	v_cvt_f32_f16_e32 v164, v61
	v_cvt_f32_f16_sdwa v165, v61 dst_sel:DWORD dst_unused:UNUSED_PAD src0_sel:WORD_1
	v_fmac_f32_e32 v142, v155, v164
	v_fmac_f32_e32 v143, v155, v165
	v_cvt_f32_f16_e32 v164, v62
	v_cvt_f32_f16_sdwa v165, v62 dst_sel:DWORD dst_unused:UNUSED_PAD src0_sel:WORD_1
	v_fmac_f32_e32 v144, v155, v164
	v_fmac_f32_e32 v145, v155, v165
	v_cvt_f32_f16_e32 v164, v63
	v_cvt_f32_f16_sdwa v165, v63 dst_sel:DWORD dst_unused:UNUSED_PAD src0_sel:WORD_1
	v_fmac_f32_e32 v146, v155, v164
	v_fmac_f32_e32 v147, v155, v165
	v_fmac_f32_e32 v166, v155, v163
	v_add_f32_dpp v140, v140, v140 row_ror:8 row_mask:0xf bank_mask:0xf
	v_add_f32_dpp v141, v141, v141 row_ror:8 row_mask:0xf bank_mask:0xf
	v_add_f32_dpp v142, v142, v142 row_ror:8 row_mask:0xf bank_mask:0xf
	v_add_f32_dpp v143, v143, v143 row_ror:8 row_mask:0xf bank_mask:0xf
	v_add_f32_dpp v144, v144, v144 row_ror:8 row_mask:0xf bank_mask:0xf
	v_add_f32_dpp v145, v145, v145 row_ror:8 row_mask:0xf bank_mask:0xf
	v_add_f32_dpp v146, v146, v146 row_ror:8 row_mask:0xf bank_mask:0xf
	v_add_f32_dpp v147, v147, v147 row_ror:8 row_mask:0xf bank_mask:0xf
	v_add_f32_dpp v166, v166, v166 row_ror:8 row_mask:0xf bank_mask:0xf
	v_add_f32_dpp v140, v140, v140 row_ror:4 row_mask:0xf bank_mask:0xf
	v_add_f32_dpp v141, v141, v141 row_ror:4 row_mask:0xf bank_mask:0xf
	v_add_f32_dpp v142, v142, v142 row_ror:4 row_mask:0xf bank_mask:0xf
	v_add_f32_dpp v143, v143, v143 row_ror:4 row_mask:0xf bank_mask:0xf
	v_add_f32_dpp v144, v144, v144 row_ror:4 row_mask:0xf bank_mask:0xf
	v_add_f32_dpp v145, v145, v145 row_ror:4 row_mask:0xf bank_mask:0xf
	v_add_f32_dpp v146, v146, v146 row_ror:4 row_mask:0xf bank_mask:0xf
	v_add_f32_dpp v147, v147, v147 row_ror:4 row_mask:0xf bank_mask:0xf
	v_add_f32_dpp v166, v166, v166 row_ror:4 row_mask:0xf bank_mask:0xf
	v_add_f32_dpp v140, v140, v140 row_ror:2 row_mask:0xf bank_mask:0xf
	v_add_f32_dpp v141, v141, v141 row_ror:2 row_mask:0xf bank_mask:0xf
	v_add_f32_dpp v142, v142, v142 row_ror:2 row_mask:0xf bank_mask:0xf
	v_add_f32_dpp v143, v143, v143 row_ror:2 row_mask:0xf bank_mask:0xf
	v_add_f32_dpp v144, v144, v144 row_ror:2 row_mask:0xf bank_mask:0xf
	v_add_f32_dpp v145, v145, v145 row_ror:2 row_mask:0xf bank_mask:0xf
	v_add_f32_dpp v146, v146, v146 row_ror:2 row_mask:0xf bank_mask:0xf
	v_add_f32_dpp v147, v147, v147 row_ror:2 row_mask:0xf bank_mask:0xf
	v_add_f32_dpp v166, v166, v166 row_ror:2 row_mask:0xf bank_mask:0xf
	v_add_f32_dpp v140, v140, v140 row_ror:1 row_mask:0xf bank_mask:0xf
	v_add_f32_dpp v141, v141, v141 row_ror:1 row_mask:0xf bank_mask:0xf
	v_add_f32_dpp v142, v142, v142 row_ror:1 row_mask:0xf bank_mask:0xf
	v_add_f32_dpp v143, v143, v143 row_ror:1 row_mask:0xf bank_mask:0xf
	v_add_f32_dpp v144, v144, v144 row_ror:1 row_mask:0xf bank_mask:0xf
	v_add_f32_dpp v145, v145, v145 row_ror:1 row_mask:0xf bank_mask:0xf
	v_add_f32_dpp v146, v146, v146 row_ror:1 row_mask:0xf bank_mask:0xf
	v_add_f32_dpp v147, v147, v147 row_ror:1 row_mask:0xf bank_mask:0xf
	v_add_f32_dpp v166, v166, v166 row_ror:1 row_mask:0xf bank_mask:0xf
	v_cvt_pk_f16_f32 v252, v140, v141
	v_cvt_pk_f16_f32 v253, v142, v143
	v_cvt_pk_f16_f32 v254, v144, v145
	v_cvt_pk_f16_f32 v255, v146, v147
	s_waitcnt lgkmcnt(0)
	v_add_f32_e32 v209, s12, v166
	v_add_u32_e32 v220, s18, v102
	v_add_u32_e32 v220, s18, v220
	v_min_u32_e32 v218, s19, v220
	v_lshlrev_b32_e32 v218, 9, v218
	v_lshl_add_u64 v[216:217], v[222:223], 0, v[218:219]
	global_load_dword v228, v[216:217], off nt
	global_load_dword v229, v[216:217], off offset:128 nt
	global_load_dword v230, v[216:217], off offset:256 nt
	global_load_dword v231, v[216:217], off offset:384 nt
	v_add_u32_e32 v220, s18, v220
	v_min_u32_e32 v218, s19, v220
	v_lshlrev_b32_e32 v218, 9, v218
	v_lshl_add_u64 v[216:217], v[222:223], 0, v[218:219]
	global_load_dword v232, v[216:217], off nt
	global_load_dword v233, v[216:217], off offset:128 nt
	global_load_dword v234, v[216:217], off offset:256 nt
	global_load_dword v235, v[216:217], off offset:384 nt
	v_add_u32_e32 v220, s18, v220
	v_min_u32_e32 v218, s19, v220
	v_lshlrev_b32_e32 v218, 9, v218
	v_lshl_add_u64 v[216:217], v[222:223], 0, v[218:219]
	global_load_dword v236, v[216:217], off nt
	global_load_dword v237, v[216:217], off offset:128 nt
	global_load_dword v238, v[216:217], off offset:256 nt
	global_load_dword v239, v[216:217], off offset:384 nt
	v_add_u32_e32 v220, s18, v220
	v_min_u32_e32 v218, s19, v220
	v_lshlrev_b32_e32 v218, 9, v218
	v_lshl_add_u64 v[216:217], v[222:223], 0, v[218:219]
	global_load_dword v240, v[216:217], off nt
	global_load_dword v241, v[216:217], off offset:128 nt
	global_load_dword v242, v[216:217], off offset:256 nt
	global_load_dword v243, v[216:217], off offset:384 nt
	v_add_u32_e32 v220, s18, v220
	v_min_u32_e32 v218, s19, v220
	v_lshlrev_b32_e32 v218, 9, v218
	v_lshl_add_u64 v[216:217], v[222:223], 0, v[218:219]
	global_load_dword v244, v[216:217], off nt
	global_load_dword v245, v[216:217], off offset:128 nt
	global_load_dword v246, v[216:217], off offset:256 nt
	global_load_dword v247, v[216:217], off offset:384 nt
	v_add_u32_e32 v220, s18, v220
	v_min_u32_e32 v218, s19, v220
	v_lshlrev_b32_e32 v218, 9, v218
	v_lshl_add_u64 v[216:217], v[222:223], 0, v[218:219]
	global_load_dword v248, v[216:217], off nt
	global_load_dword v249, v[216:217], off offset:128 nt
	global_load_dword v250, v[216:217], off offset:256 nt
	global_load_dword v251, v[216:217], off offset:384 nt
	s_waitcnt vmcnt(24)
